# GLA item loops (G1, G3): loop-invariant gate weights loaded once and kept in spare VGPRs, next item's gate inputs prefetched one item ahead (no exposed vmcnt(0) at the item start)
# baseline (speedup 1.0000x reference)
; #define INP(k) ldptr(PTAB, (k))
; __global__ void __launch_bounds__(NWAVES * 64, 2) fwd_kernel(Args args) {
;     ...
;             { BODY_LOCALS
;               for (int it = vcu; it < 1024; it += G) { float wa[16], ba; gla_alpha_load(wa, ba, INP(6) + (size_t)l * 16 * 512, INP(7) + l * 512, (it >> 6) & 3, tid);
;                   const GlaPre cur = gla_blr_load(WSP(WS_ZABC), (size_t)(it >> 8) * SEQ + 64 * (it & 63), tid);
;                   gla_g1(ring, WSP(WS_ZABC), ((bf16*)xo), (float*)(ws + WS_GLADEC), cur, wa, ba, it, tid); } }
.LBB0_913:
	s_or_b64 exec, exec, s[38:39]
	s_lshl_b32 s0, s88, 9
	s_mov_b32 s1, s95
	v_writelane_b32 v255, s0, 31
	v_readlane_b32 s12, v252, 6
	v_readlane_b32 s8, v252, 4
	v_writelane_b32 v255, s1, 32
	v_readlane_b32 s18, v252, 12
	v_readlane_b32 s19, v252, 13
	v_readlane_b32 s0, v252, 32
	v_readlane_b32 s9, v252, 5
	s_mov_b64 s[4:5], s[18:19]
	v_readlane_b32 s1, v252, 33
	s_waitcnt lgkmcnt(0)
	s_barrier
	s_lshl_b32 s50, s88, 13
	s_mov_b32 s51, s95
	v_mbcnt_lo_u32_b32 v0, -1, 0
	v_mbcnt_hi_u32_b32 v0, -1, v0
	s_andn2_b64 vcc, exec, s[0:1]
	v_readlane_b32 s13, v252, 7
	v_readlane_b32 s14, v252, 8
	v_readlane_b32 s15, v252, 9
	v_readlane_b32 s16, v252, 10
	v_readlane_b32 s17, v252, 11
	v_mbcnt_lo_u32_b32 v0, -1, 0
	v_mbcnt_hi_u32_b32 v0, -1, v0
	s_cbranch_vccnz .LBB0_924
	v_readlane_b32 s0, v252, 37
	s_add_u32 s6, s8, 0x15600000
	s_addc_u32 s7, s9, 0
	v_add_u32_e32 v72, s0, v0
	v_readlane_b32 s0, v254, 14
	v_ashrrev_i32_e32 v66, 4, v72
	v_and_b32_e32 v0, 15, v0
	s_add_u32 s10, s8, s0
	v_readlane_b32 s0, v254, 15
	v_readlane_b32 s12, v254, 8
	v_readlane_b32 s14, v254, 12
	v_and_b32_e32 v73, 0x7f, v72
	v_ashrrev_i32_e32 v67, 31, v66
	s_addc_u32 s11, s9, s0
	v_lshlrev_b32_e32 v68, 1, v0
	v_readlane_b32 s13, v254, 9
	v_readlane_b32 s0, v253, 58
	s_mov_b32 s1, s14
	v_readlane_b32 s15, v254, 13
	s_mov_b32 s32, 0
	s_branch .LBB0_916

; __device__ __forceinline__ void gla_alpha_load(float (&wa)[16], float& ba, const float* w_alpha, const float* b_alpha, int h, int tid) {
;     const int k = tid & 127;
; #pragma unroll
;     for (int j = 0; j < 16; ++j) wa[j] = w_alpha[j * 512 + h * 128 + k];
;     ba = b_alpha[h * 128 + k];
; }
.LBB0_916:
	v_readlane_b32 s14, v254, 43
	v_mov_b64_e32 v[14:15], s[6:7]
	s_movk_i32 s22, 0x2200
	v_mov_b32_e32 v0, s14
	ds_read_b64 v[2:3], v0
	s_lshl_b64 s[14:15], s[50:51], 2
	v_mov_b32_e32 v69, v1
	v_mov_b32_e32 v70, v72
	v_mov_b32_e32 v17, v1
	s_waitcnt lgkmcnt(0)
	v_readfirstlane_b32 s16, v2
	s_add_u32 s16, s16, s14
	v_readlane_b32 s14, v254, 44
	v_readfirstlane_b32 s17, v3
	s_addc_u32 s17, s17, s15
	v_mov_b32_e32 v0, s14
	ds_read_b64 v[2:3], v0
	v_readlane_b32 s14, v255, 31
	v_readlane_b32 s15, v255, 32
	s_lshl_b64 s[14:15], s[14:15], 2
	s_waitcnt lgkmcnt(0)
	v_readfirstlane_b32 s18, v2
	v_readfirstlane_b32 s19, v3
	s_add_u32 s18, s18, s14
	s_addc_u32 s19, s19, s15
	s_bfe_u32 s15, s1, 0x20006
	s_lshl_b32 s14, s15, 9
	s_cmp_eq_u32 s32, 0
	s_cselect_b64 exec, -1, 0
	v_lshl_or_b32 v0, v73, 2, s14
	v_lshl_add_u64 v[2:3], s[16:17], 0, v[0:1]
	v_add_co_u32_e32 v4, vcc, s43, v2
	global_load_dword v51, v0, s[16:17]
	global_load_dword v54, v0, s[16:17] offset:2048
	v_addc_co_u32_e32 v5, vcc, 0, v3, vcc
	v_add_co_u32_e32 v6, vcc, s84, v2
	s_movk_i32 s16, 0x4000
	s_nop 0
	v_addc_co_u32_e32 v7, vcc, 0, v3, vcc
	global_load_dword v58, v[6:7], off offset:-4096
	global_load_dword v55, v[4:5], off offset:2048
	global_load_dword v52, v[6:7], off
	global_load_dword v56, v[6:7], off offset:2048
	v_add_co_u32_e32 v4, vcc, s37, v2
	s_lshl_b32 s94, s15, 8
	s_nop 0
	v_addc_co_u32_e32 v5, vcc, 0, v3, vcc
	v_add_co_u32_e32 v6, vcc, s16, v2
	s_movk_i32 s16, 0x5000
	s_nop 0
	v_addc_co_u32_e32 v7, vcc, 0, v3, vcc
	global_load_dword v61, v[6:7], off offset:-4096
	global_load_dword v59, v[4:5], off offset:2048
	global_load_dword v53, v[6:7], off
	global_load_dword v60, v[6:7], off offset:2048
	v_add_co_u32_e32 v4, vcc, s16, v2
	s_movk_i32 s16, 0x6000
	s_nop 0
	v_addc_co_u32_e32 v5, vcc, 0, v3, vcc
	v_add_co_u32_e32 v6, vcc, s16, v2
	s_movk_i32 s16, 0x7000
	s_nop 0
	v_addc_co_u32_e32 v7, vcc, 0, v3, vcc
	v_add_co_u32_e32 v2, vcc, s16, v2
	s_ashr_i32 s16, s1, 8
	s_nop 0
	v_addc_co_u32_e32 v3, vcc, 0, v3, vcc
	s_ashr_i32 s17, s16, 31
	global_load_dword v71, v[6:7], off offset:-4096
	global_load_dword v63, v[4:5], off offset:2048
	global_load_dword v57, v[6:7], off
	global_load_dword v64, v[6:7], off offset:2048
	global_load_dword v65, v[2:3], off
	global_load_dword v62, v[2:3], off offset:2048
	global_load_dword v74, v0, s[18:19]
	s_mov_b64 exec, -1
	s_lshl_b64 s[16:17], s[16:17], 12
	s_and_b32 s18, s0, 0xfc0
	s_or_b32 s16, s16, s18
	v_lshl_add_u64 v[2:3], s[16:17], 0, v[66:67]
	v_mad_u64_u32 v[4:5], s[18:19], v2, s22, v[14:15]
	v_mad_i32_i24 v5, v3, s22, v5
	v_lshl_add_u64 v[2:3], v[4:5], 0, v[68:69]
	s_mov_b32 s18, 0x46000
	v_add_co_u32_e32 v4, vcc, s18, v2
	s_mov_b32 s15, s95
	s_nop 0
	v_addc_co_u32_e32 v5, vcc, 0, v3, vcc
	s_cmp_eq_u32 s32, 0
	s_cselect_b64 exec, -1, 0
	global_load_ushort v0, v[4:5], off offset:128
	s_mov_b64 exec, -1
	v_add_co_u32_e32 v2, vcc, s84, v2
	s_nop 1
	v_addc_co_u32_e32 v3, vcc, 0, v3, vcc
	s_cmp_eq_u32 s32, 0
	s_cselect_b64 exec, -1, 0
	global_load_ushort v29, v[2:3], off offset:128
	s_mov_b64 exec, -1
	s_cmp_eq_u32 s32, 0
	s_cbranch_scc1 .Lg1_first
	v_mov_b32_e32 v0, v197
	v_mov_b32_e32 v29, v198
	v_mov_b32_e32 v51, v180
	v_mov_b32_e32 v54, v181
	v_mov_b32_e32 v58, v182
	v_mov_b32_e32 v55, v183
	v_mov_b32_e32 v52, v184
	v_mov_b32_e32 v56, v185
	v_mov_b32_e32 v61, v186
	v_mov_b32_e32 v59, v187
	v_mov_b32_e32 v53, v188
	v_mov_b32_e32 v60, v189
	v_mov_b32_e32 v71, v190
	v_mov_b32_e32 v63, v191
	v_mov_b32_e32 v57, v192
	v_mov_b32_e32 v64, v193
	v_mov_b32_e32 v65, v194
	v_mov_b32_e32 v62, v195
	v_mov_b32_e32 v74, v196
	s_branch .Lg1_pf
.Lg1_first:
	s_waitcnt vmcnt(0)
	v_mov_b32_e32 v180, v51
	v_mov_b32_e32 v181, v54
	v_mov_b32_e32 v182, v58
	v_mov_b32_e32 v183, v55
	v_mov_b32_e32 v184, v52
	v_mov_b32_e32 v185, v56
	v_mov_b32_e32 v186, v61
	v_mov_b32_e32 v187, v59
	v_mov_b32_e32 v188, v53
	v_mov_b32_e32 v189, v60
	v_mov_b32_e32 v190, v71
	v_mov_b32_e32 v191, v63
	v_mov_b32_e32 v192, v57
	v_mov_b32_e32 v193, v64
	v_mov_b32_e32 v194, v65
	v_mov_b32_e32 v195, v62
	v_mov_b32_e32 v196, v74
	s_mov_b32 s32, 1
.Lg1_pf:
	s_add_i32 s98, s1, s78
	s_cmpk_gt_i32 s98, 0x3ff
	s_cbranch_scc1 .Lg1_join
	s_mov_b64 s[98:99], 0x2200000
	v_lshl_add_u64 v[200:201], v[4:5], 0, s[98:99]
	global_load_ushort v197, v[200:201], off offset:128
	v_lshl_add_u64 v[200:201], v[2:3], 0, s[98:99]
	global_load_ushort v198, v[200:201], off offset:128
; #define LAS __attribute__((address_space(3)))
; __device__ __forceinline__ void gla_cum(LAS unsigned char* lds, const GlaPre pre, const float (&wa)[16], const float ba, int tid) {
;     LAS float* cum = (LAS float*)(lds + GL_CUM); LAS float* blr = (LAS float*)(lds + GL_BLR); LAS float* tot = blr + 1024;
;     blr[tid] = __uint_as_float((unsigned)pre.b0 << 16); blr[tid + 512] = __uint_as_float((unsigned)pre.b1 << 16);
;     const int k = tid & 127, q = tid >> 7;
;     __syncthreads();
;     float c[16]; float run = 0.f;
; #pragma unroll
;     for (int i2 = 0; i2 < 16; i2 += 4) {
;         f32x4 bb[16];
; #pragma unroll
;         for (int e = 0; e < 16; ++e) bb[e] = *(const LAS f32x4*)(blr + (16 * q + i2 + (e >> 2)) * 16 + 4 * (e & 3));
;         asm volatile("" : "+v"(bb[0]), "+v"(bb[1]), "+v"(bb[2]), "+v"(bb[3]), "+v"(bb[4]), "+v"(bb[5]), "+v"(bb[6]), "+v"(bb[7]), "+v"(bb[8]), "+v"(bb[9]), "+v"(bb[10]), "+v"(bb[11]), "+v"(bb[12]), "+v"(bb[13]), "+v"(bb[14]), "+v"(bb[15]) :: "memory");
; #pragma unroll
;         for (int ii = 0; ii < 4; ++ii) { float x = ba;
; #pragma unroll
;             for (int j4 = 0; j4 < 4; ++j4) { const f32x4 b4 = bb[ii * 4 + j4]; x += b4.x * wa[4 * j4] + b4.y * wa[4 * j4 + 1] + b4.z * wa[4 * j4 + 2] + b4.w * wa[4 * j4 + 3]; }
;             const float ls = fminf(x, 0.f) - 0.6931471805599453f * __builtin_amdgcn_logf(1.0f + __builtin_amdgcn_exp2f(-1.4426950408889634f * fabsf(x)));
;             run += ls * (1.0f / 16.0f); c[i2 + ii] = run; } }
; __device__ __forceinline__ void gla_g1(LAS unsigned char* lds, const bf16* Z, bf16* ST, float* DEC, const GlaPre pre, const float (&wa)[16], const float ba, int item, int tid) {
;     ...
;     v4u kraw[2];
; #pragma unroll
;     for (int i = 0; i < 2; ++i) { const int t = (tid >> 4) + 32 * i, kc = (tid & 15) * 8; kraw[i] = *(const v4u*)(Z + (m0 + t) * NABC + ZC_BK + h * 128 + kc); }
;     const GlaV vraw = gla_load_v(Z, m0, h, tid);
.Lg1_join:
	v_lshlrev_b32_e32 v28, 16, v0
	v_ashrrev_i32_e32 v38, 4, v70
	v_ashrrev_i32_e32 v39, 31, v38
	v_lshl_add_u64 v[2:3], s[16:17], 0, v[38:39]
	v_lshlrev_b32_e32 v50, 3, v70
	v_mad_u64_u32 v[4:5], s[20:21], v2, s22, v[14:15]
	v_and_b32_e32 v69, 0x78, v50
	v_mad_i32_i24 v5, v3, s22, v5
	v_lshl_add_u64 v[2:3], v[4:5], 0, s[94:95]
	v_lshlrev_b32_e32 v0, 1, v69
	v_add_u32_e32 v40, 32, v38
	v_lshl_add_u64 v[2:3], v[2:3], 0, v[0:1]
	v_ashrrev_i32_e32 v41, 31, v40
	global_load_dwordx4 v[22:25], v[2:3], off offset:1024
	v_lshl_add_u64 v[2:3], s[16:17], 0, v[40:41]
	v_add_u32_e32 v41, 0x200, v70
	v_ashrrev_i32_e32 v44, 5, v41
	v_ashrrev_i32_e32 v45, 31, v44
	v_lshl_add_u64 v[6:7], s[16:17], 0, v[44:45]
	v_mad_u64_u32 v[4:5], s[20:21], v2, s22, v[14:15]
	v_mad_u64_u32 v[8:9], s[20:21], v6, s22, v[14:15]
	v_mad_i32_i24 v5, v3, s22, v5
	v_lshlrev_b32_e32 v39, 4, v70
	v_mad_i32_i24 v9, v7, s22, v9
	v_lshl_add_u64 v[2:3], v[4:5], 0, s[94:95]
	v_ashrrev_i32_e32 v42, 5, v70
	v_and_b32_e32 v16, 0x1f0, v39
	v_lshl_add_u64 v[6:7], v[8:9], 0, s[14:15]
	v_lshl_add_u64 v[2:3], v[2:3], 0, v[0:1]
	v_ashrrev_i32_e32 v43, 31, v42
	v_lshl_add_u64 v[6:7], v[6:7], 0, v[16:17]
	global_load_dwordx4 v[18:21], v[2:3], off offset:1024
	v_add_u32_e32 v45, 0x600, v70
	global_load_dwordx4 v[6:9], v[6:7], off offset:2048
	v_lshl_add_u64 v[2:3], s[16:17], 0, v[42:43]
	v_add_u32_e32 v43, 0x400, v70
	v_ashrrev_i32_e32 v46, 5, v43
	v_ashrrev_i32_e32 v48, 5, v45
	v_ashrrev_i32_e32 v47, 31, v46
	v_ashrrev_i32_e32 v49, 31, v48
	v_lshl_add_u64 v[10:11], s[16:17], 0, v[46:47]
	v_lshl_add_u64 v[26:27], s[16:17], 0, v[48:49]
	v_mad_u64_u32 v[4:5], s[20:21], v2, s22, v[14:15]
	v_mad_u64_u32 v[12:13], s[20:21], v10, s22, v[14:15]
	v_mad_u64_u32 v[14:15], s[16:17], v26, s22, v[14:15]
	v_mad_i32_i24 v5, v3, s22, v5
	v_mad_i32_i24 v13, v11, s22, v13
	v_mad_i32_i24 v15, v27, s22, v15
	v_lshl_add_u64 v[2:3], v[4:5], 0, s[14:15]
	v_lshl_add_u64 v[10:11], v[12:13], 0, s[14:15]
	v_lshl_add_u64 v[14:15], v[14:15], 0, s[14:15]
	s_add_i32 s14, 0, 0x18000
	v_lshlrev_b32_e32 v49, 2, v70
	v_ashrrev_i32_e32 v47, 7, v70
	v_lshl_add_u64 v[2:3], v[2:3], 0, v[16:17]
	v_lshl_add_u64 v[10:11], v[10:11], 0, v[16:17]
	v_lshl_add_u64 v[14:15], v[14:15], 0, v[16:17]
	v_lshlrev_b32_e32 v26, 16, v29
	v_add_u32_e32 v27, s14, v49
	v_lshl_add_u32 v80, v47, 10, s14
	global_load_dwordx4 v[2:5], v[2:3], off offset:2048
	ds_write2st64_b32 v27, v26, v28 offset1:8
	global_load_dwordx4 v[10:13], v[10:11], off offset:2048
	s_mov_b32 s14, 0xbfb8aa3b
	global_load_dwordx4 v[14:17], v[14:15], off offset:2048
	s_waitcnt lgkmcnt(0)
	s_barrier
	ds_read_b128 v[26:29], v80 offset:240
	ds_read_b128 v[30:33], v80 offset:224
	ds_read_b128 v[34:37], v80 offset:208
	ds_read_b128 v[82:85], v80 offset:192
	ds_read_b128 v[86:89], v80 offset:176
	ds_read_b128 v[90:93], v80 offset:160
	ds_read_b128 v[94:97], v80 offset:144
	ds_read_b128 v[98:101], v80 offset:128
	ds_read_b128 v[102:105], v80 offset:112
	ds_read_b128 v[106:109], v80 offset:96
	ds_read_b128 v[110:113], v80 offset:80
	ds_read_b128 v[114:117], v80 offset:64
	ds_read_b128 v[76:79], v80
	ds_read_b128 v[118:121], v80 offset:16
	ds_read_b128 v[122:125], v80 offset:32
	ds_read_b128 v[126:129], v80 offset:48
	s_waitcnt lgkmcnt(0)
	s_nop 0
	v_mul_f32_e32 v75, v54, v77
	v_fmac_f32_e32 v75, v51, v76
	v_mul_f32_e32 v76, v56, v119
	v_fmac_f32_e32 v75, v58, v78
	v_fmac_f32_e32 v76, v52, v118
	v_fmac_f32_e32 v75, v55, v79
	v_fmac_f32_e32 v76, v61, v120
	v_add_f32_e32 v75, v74, v75
	v_fmac_f32_e32 v76, v59, v121
	v_add_f32_e32 v75, v76, v75
	v_mul_f32_e32 v76, v60, v123
	v_fmac_f32_e32 v76, v53, v122
	v_fmac_f32_e32 v76, v71, v124
	v_fmac_f32_e32 v76, v63, v125
	v_add_f32_e32 v75, v76, v75
	v_mul_f32_e32 v76, v64, v127
	v_fmac_f32_e32 v76, v57, v126
	v_fmac_f32_e32 v76, v65, v128
	v_fmac_f32_e32 v76, v62, v129
	v_add_f32_e32 v76, v76, v75
	v_min_f32_e32 v77, 0, v76
	v_mul_f32_e64 v76, |v76|, s14
	v_exp_f32_e32 v76, v76
	s_mov_b32 s15, 0x3d800000
	v_mul_f32_e32 v78, v56, v111
	v_fmac_f32_e32 v78, v52, v110
	v_add_f32_e32 v76, 1.0, v76
	v_log_f32_e32 v76, v76
	v_fmac_f32_e32 v78, v61, v112
	v_fmac_f32_e32 v78, v59, v113
	v_mul_f32_e32 v79, v56, v95
	v_fmac_f32_e32 v77, 0xbf317218, v76
	v_fma_f32 v76, v77, s15, 0
	v_mul_f32_e32 v77, v54, v115
	v_fmac_f32_e32 v77, v51, v114
	v_fmac_f32_e32 v77, v58, v116
	v_fmac_f32_e32 v77, v55, v117
	v_add_f32_e32 v77, v74, v77
	v_add_f32_e32 v77, v78, v77
	v_mul_f32_e32 v78, v60, v107
	v_fmac_f32_e32 v78, v53, v106
	v_fmac_f32_e32 v78, v71, v108
	v_fmac_f32_e32 v78, v63, v109
	v_add_f32_e32 v77, v78, v77
	v_mul_f32_e32 v78, v64, v103
	v_fmac_f32_e32 v78, v57, v102
	v_fmac_f32_e32 v78, v65, v104
	v_fmac_f32_e32 v78, v62, v105
	v_add_f32_e32 v77, v78, v77
	v_min_f32_e32 v78, 0, v77
	v_mul_f32_e64 v77, |v77|, s14
	v_exp_f32_e32 v77, v77
	v_fmac_f32_e32 v79, v52, v94
	v_fmac_f32_e32 v79, v61, v96
	v_fmac_f32_e32 v79, v59, v97
	v_add_f32_e32 v77, 1.0, v77
	v_log_f32_e32 v77, v77
	v_mul_f32_e32 v35, v56, v35
	v_fmac_f32_e32 v35, v52, v34
	v_mul_f32_e32 v31, v60, v31
	v_fmac_f32_e32 v78, 0xbf317218, v77
	v_fmamk_f32 v77, v78, 0x3d800000, v76
	v_mul_f32_e32 v78, v54, v99
	v_fmac_f32_e32 v78, v51, v98
	v_fmac_f32_e32 v78, v58, v100
	v_fmac_f32_e32 v78, v55, v101
	v_add_f32_e32 v78, v74, v78
	v_add_f32_e32 v78, v79, v78
	v_mul_f32_e32 v79, v60, v91
	v_fmac_f32_e32 v79, v53, v90
	v_fmac_f32_e32 v79, v71, v92
	v_fmac_f32_e32 v79, v63, v93
	v_add_f32_e32 v78, v79, v78
	v_mul_f32_e32 v79, v64, v87
	v_fmac_f32_e32 v79, v57, v86
	v_fmac_f32_e32 v79, v65, v88
	v_fmac_f32_e32 v79, v62, v89
	v_add_f32_e32 v78, v79, v78
	v_min_f32_e32 v79, 0, v78
	v_mul_f32_e64 v78, |v78|, s14
; #define LAS __attribute__((address_space(3)))
; __device__ __forceinline__ void gla_cum(LAS unsigned char* lds, const GlaPre pre, const float (&wa)[16], const float ba, int tid) {
;     ...
;     for (int i2 = 0; i2 < 16; i2 += 4) {
;         f32x4 bb[16];
; #pragma unroll
;         for (int e = 0; e < 16; ++e) bb[e] = *(const LAS f32x4*)(blr + (16 * q + i2 + (e >> 2)) * 16 + 4 * (e & 3));
;         asm volatile("" : "+v"(bb[0]), "+v"(bb[1]), "+v"(bb[2]), "+v"(bb[3]), "+v"(bb[4]), "+v"(bb[5]), "+v"(bb[6]), "+v"(bb[7]), "+v"(bb[8]), "+v"(bb[9]), "+v"(bb[10]), "+v"(bb[11]), "+v"(bb[12]), "+v"(bb[13]), "+v"(bb[14]), "+v"(bb[15]) :: "memory");
; #pragma unroll
;         for (int ii = 0; ii < 4; ++ii) { float x = ba;
; #pragma unroll
;             for (int j4 = 0; j4 < 4; ++j4) { const f32x4 b4 = bb[ii * 4 + j4]; x += b4.x * wa[4 * j4] + b4.y * wa[4 * j4 + 1] + b4.z * wa[4 * j4 + 2] + b4.w * wa[4 * j4 + 3]; }
;             const float ls = fminf(x, 0.f) - 0.6931471805599453f * __builtin_amdgcn_logf(1.0f + __builtin_amdgcn_exp2f(-1.4426950408889634f * fabsf(x)));
;             run += ls * (1.0f / 16.0f); c[i2 + ii] = run; } }
	v_exp_f32_e32 v78, v78
	v_fmac_f32_e32 v35, v61, v36
	v_fmac_f32_e32 v31, v53, v30
	v_mul_f32_e32 v27, v64, v27
	v_add_f32_e32 v78, 1.0, v78
	v_log_f32_e32 v78, v78
	v_fmac_f32_e32 v35, v59, v37
	v_fmac_f32_e32 v31, v71, v32
	v_fmac_f32_e32 v27, v57, v26
	v_fmac_f32_e32 v79, 0xbf317218, v78
	v_fmamk_f32 v78, v79, 0x3d800000, v77
	v_mul_f32_e32 v79, v54, v83
	v_fmac_f32_e32 v79, v51, v82
	v_fmac_f32_e32 v79, v58, v84
	v_fmac_f32_e32 v79, v55, v85
	v_add_f32_e32 v79, v74, v79
	v_add_f32_e32 v34, v35, v79
	v_fmac_f32_e32 v31, v63, v33
	v_fmac_f32_e32 v27, v65, v28
	v_add_f32_e32 v30, v31, v34
	v_fmac_f32_e32 v27, v62, v29
	v_add_f32_e32 v26, v27, v30
	v_min_f32_e32 v27, 0, v26
	v_mul_f32_e64 v26, |v26|, s14
	v_exp_f32_e32 v26, v26
	v_readfirstlane_b32 s18, v70
	v_mov_b32_e32 v75, 0
	v_cmp_lt_i32_e32 vcc, 0, v47
	v_add_f32_e32 v26, 1.0, v26
	v_log_f32_e32 v26, v26
	s_nop 0
	v_fmac_f32_e32 v27, 0xbf317218, v26
	v_fmamk_f32 v79, v27, 0x3d800000, v78
	ds_read_b128 v[26:29], v80 offset:496
	ds_read_b128 v[30:33], v80 offset:480
	ds_read_b128 v[34:37], v80 offset:464
	ds_read_b128 v[84:87], v80 offset:448
	ds_read_b128 v[88:91], v80 offset:432
	ds_read_b128 v[92:95], v80 offset:416
	ds_read_b128 v[96:99], v80 offset:400
	ds_read_b128 v[100:103], v80 offset:384
	ds_read_b128 v[104:107], v80 offset:368
	ds_read_b128 v[108:111], v80 offset:352
	ds_read_b128 v[112:115], v80 offset:336
	ds_read_b128 v[116:119], v80 offset:320
	ds_read_b128 v[120:123], v80 offset:256
	ds_read_b128 v[124:127], v80 offset:272
	ds_read_b128 v[128:131], v80 offset:288
	ds_read_b128 v[132:135], v80 offset:304
	s_waitcnt lgkmcnt(0)
	s_nop 0
	v_mul_f32_e32 v81, v54, v121
	v_fmac_f32_e32 v81, v51, v120
	v_mul_f32_e32 v82, v56, v125
	v_fmac_f32_e32 v81, v58, v122
	v_fmac_f32_e32 v82, v52, v124
	v_fmac_f32_e32 v81, v55, v123
	v_fmac_f32_e32 v82, v61, v126
	v_add_f32_e32 v81, v74, v81
	v_fmac_f32_e32 v82, v59, v127
	v_add_f32_e32 v81, v82, v81
	v_mul_f32_e32 v82, v60, v129
	v_fmac_f32_e32 v82, v53, v128
	v_fmac_f32_e32 v82, v71, v130
	v_fmac_f32_e32 v82, v63, v131
	v_add_f32_e32 v81, v82, v81
	v_mul_f32_e32 v82, v64, v133
	v_fmac_f32_e32 v82, v57, v132
	v_fmac_f32_e32 v82, v65, v134
	v_fmac_f32_e32 v82, v62, v135
	v_add_f32_e32 v81, v82, v81
	v_min_f32_e32 v82, 0, v81
	v_mul_f32_e64 v81, |v81|, s14
	v_exp_f32_e32 v81, v81
	v_mul_f32_e32 v83, v56, v113
	v_fmac_f32_e32 v83, v52, v112
	v_fmac_f32_e32 v83, v61, v114
	v_add_f32_e32 v81, 1.0, v81
	v_log_f32_e32 v81, v81
	v_fmac_f32_e32 v83, v59, v115
	v_mul_f32_e32 v97, v56, v97
	v_mul_f32_e32 v85, v54, v85
	v_fmac_f32_e32 v82, 0xbf317218, v81
	v_fmamk_f32 v81, v82, 0x3d800000, v79
	v_mul_f32_e32 v82, v54, v117
	v_fmac_f32_e32 v82, v51, v116
	v_fmac_f32_e32 v82, v58, v118
	v_fmac_f32_e32 v82, v55, v119
	v_add_f32_e32 v82, v74, v82
	v_add_f32_e32 v82, v83, v82
	v_mul_f32_e32 v83, v60, v109
	v_fmac_f32_e32 v83, v53, v108
	v_fmac_f32_e32 v83, v71, v110
	v_fmac_f32_e32 v83, v63, v111
	v_add_f32_e32 v82, v83, v82
	v_mul_f32_e32 v83, v64, v105
	v_fmac_f32_e32 v83, v57, v104
	v_fmac_f32_e32 v83, v65, v106
	v_fmac_f32_e32 v83, v62, v107
	v_add_f32_e32 v82, v83, v82
	v_min_f32_e32 v83, 0, v82
	v_mul_f32_e64 v82, |v82|, s14
	v_exp_f32_e32 v82, v82
	v_fmac_f32_e32 v97, v52, v96
	v_mul_f32_e32 v93, v60, v93
	v_fmac_f32_e32 v85, v51, v84
	v_add_f32_e32 v82, 1.0, v82
	v_log_f32_e32 v82, v82
	v_mul_f32_e32 v35, v56, v35
	v_fmac_f32_e32 v97, v61, v98
	v_fmac_f32_e32 v93, v53, v92
	v_fmac_f32_e32 v83, 0xbf317218, v82
	v_fmamk_f32 v82, v83, 0x3d800000, v81
	v_mul_f32_e32 v83, v54, v101
	v_fmac_f32_e32 v83, v51, v100
	v_fmac_f32_e32 v83, v58, v102
	v_fmac_f32_e32 v83, v55, v103
	v_mul_f32_e32 v89, v64, v89
	v_fmac_f32_e32 v85, v58, v86
	v_fmac_f32_e32 v35, v52, v34
	v_mul_f32_e32 v31, v60, v31
	v_add_f32_e32 v83, v74, v83
	v_fmac_f32_e32 v97, v59, v99
	v_fmac_f32_e32 v93, v71, v94
	v_fmac_f32_e32 v89, v57, v88
	v_fmac_f32_e32 v85, v55, v87
	v_fmac_f32_e32 v35, v61, v36
	v_fmac_f32_e32 v31, v53, v30
	v_mul_f32_e32 v27, v64, v27
	v_add_f32_e32 v83, v97, v83
	v_fmac_f32_e32 v93, v63, v95
	v_fmac_f32_e32 v89, v65, v90
	v_add_f32_e32 v84, v74, v85
	v_fmac_f32_e32 v35, v59, v37
	v_fmac_f32_e32 v31, v71, v32
	v_fmac_f32_e32 v27, v57, v26
	v_add_f32_e32 v83, v93, v83
	v_fmac_f32_e32 v89, v62, v91
	v_add_f32_e32 v34, v35, v84
	v_fmac_f32_e32 v31, v63, v33
	v_fmac_f32_e32 v27, v65, v28
	v_add_f32_e32 v83, v89, v83
	v_add_f32_e32 v30, v31, v34
	v_fmac_f32_e32 v27, v62, v29
	v_min_f32_e32 v88, 0, v83
	v_mul_f32_e64 v83, |v83|, s14
	v_add_f32_e32 v26, v27, v30
	v_exp_f32_e32 v83, v83
	v_min_f32_e32 v27, 0, v26
	v_mul_f32_e64 v26, |v26|, s14
	v_exp_f32_e32 v26, v26
	v_add_f32_e32 v83, 1.0, v83
	v_log_f32_e32 v83, v83
	v_add_f32_e32 v26, 1.0, v26
	v_log_f32_e32 v26, v26
	v_fmac_f32_e32 v88, 0xbf317218, v83
	v_fmamk_f32 v83, v88, 0x3d800000, v82
	v_fmac_f32_e32 v27, 0xbf317218, v26
	v_fmamk_f32 v84, v27, 0x3d800000, v83
	ds_read_b128 v[26:29], v80 offset:752
	ds_read_b128 v[30:33], v80 offset:736
	ds_read_b128 v[34:37], v80 offset:720
	ds_read_b128 v[88:91], v80 offset:704
	ds_read_b128 v[92:95], v80 offset:688
	ds_read_b128 v[96:99], v80 offset:672
	ds_read_b128 v[100:103], v80 offset:656
	ds_read_b128 v[104:107], v80 offset:640
	ds_read_b128 v[108:111], v80 offset:624
	ds_read_b128 v[112:115], v80 offset:608
	ds_read_b128 v[116:119], v80 offset:592
	ds_read_b128 v[120:123], v80 offset:576
	ds_read_b128 v[124:127], v80 offset:512
	ds_read_b128 v[128:131], v80 offset:528
	ds_read_b128 v[132:135], v80 offset:544
	ds_read_b128 v[136:139], v80 offset:560
	s_waitcnt lgkmcnt(0)
; #define LAS __attribute__((address_space(3)))
; __device__ __forceinline__ void gla_cum(LAS unsigned char* lds, const GlaPre pre, const float (&wa)[16], const float ba, int tid) {
;     ...
;     for (int i2 = 0; i2 < 16; i2 += 4) {
;         f32x4 bb[16];
; #pragma unroll
;         for (int e = 0; e < 16; ++e) bb[e] = *(const LAS f32x4*)(blr + (16 * q + i2 + (e >> 2)) * 16 + 4 * (e & 3));
;         asm volatile("" : "+v"(bb[0]), "+v"(bb[1]), "+v"(bb[2]), "+v"(bb[3]), "+v"(bb[4]), "+v"(bb[5]), "+v"(bb[6]), "+v"(bb[7]), "+v"(bb[8]), "+v"(bb[9]), "+v"(bb[10]), "+v"(bb[11]), "+v"(bb[12]), "+v"(bb[13]), "+v"(bb[14]), "+v"(bb[15]) :: "memory");
; #pragma unroll
;         for (int ii = 0; ii < 4; ++ii) { float x = ba;
; #pragma unroll
;             for (int j4 = 0; j4 < 4; ++j4) { const f32x4 b4 = bb[ii * 4 + j4]; x += b4.x * wa[4 * j4] + b4.y * wa[4 * j4 + 1] + b4.z * wa[4 * j4 + 2] + b4.w * wa[4 * j4 + 3]; }
;             const float ls = fminf(x, 0.f) - 0.6931471805599453f * __builtin_amdgcn_logf(1.0f + __builtin_amdgcn_exp2f(-1.4426950408889634f * fabsf(x)));
;             run += ls * (1.0f / 16.0f); c[i2 + ii] = run; } }
	s_nop 0
	v_mul_f32_e32 v85, v54, v125
	v_fmac_f32_e32 v85, v51, v124
	v_mul_f32_e32 v86, v56, v129
	v_fmac_f32_e32 v85, v58, v126
	v_fmac_f32_e32 v86, v52, v128
	v_fmac_f32_e32 v85, v55, v127
	v_fmac_f32_e32 v86, v61, v130
	v_add_f32_e32 v85, v74, v85
	v_fmac_f32_e32 v86, v59, v131
	v_add_f32_e32 v85, v86, v85
	v_mul_f32_e32 v86, v60, v133
	v_fmac_f32_e32 v86, v53, v132
	v_fmac_f32_e32 v86, v71, v134
	v_fmac_f32_e32 v86, v63, v135
	v_add_f32_e32 v85, v86, v85
	v_mul_f32_e32 v86, v64, v137
	v_fmac_f32_e32 v86, v57, v136
	v_fmac_f32_e32 v86, v65, v138
	v_fmac_f32_e32 v86, v62, v139
	v_add_f32_e32 v85, v86, v85
	v_min_f32_e32 v86, 0, v85
	v_mul_f32_e64 v85, |v85|, s14
	v_exp_f32_e32 v85, v85
	v_mul_f32_e32 v87, v56, v117
	v_fmac_f32_e32 v87, v52, v116
	v_fmac_f32_e32 v87, v61, v118
	v_add_f32_e32 v85, 1.0, v85
	v_log_f32_e32 v85, v85
	v_fmac_f32_e32 v87, v59, v119
	v_mul_f32_e32 v101, v56, v101
	v_mul_f32_e32 v89, v54, v89
	v_fmac_f32_e32 v86, 0xbf317218, v85
	v_fmamk_f32 v85, v86, 0x3d800000, v84
	v_mul_f32_e32 v86, v54, v121
	v_fmac_f32_e32 v86, v51, v120
	v_fmac_f32_e32 v86, v58, v122
	v_fmac_f32_e32 v86, v55, v123
	v_add_f32_e32 v86, v74, v86
	v_add_f32_e32 v86, v87, v86
	v_mul_f32_e32 v87, v60, v113
	v_fmac_f32_e32 v87, v53, v112
	v_fmac_f32_e32 v87, v71, v114
	v_fmac_f32_e32 v87, v63, v115
	v_add_f32_e32 v86, v87, v86
	v_mul_f32_e32 v87, v64, v109
	v_fmac_f32_e32 v87, v57, v108
	v_fmac_f32_e32 v87, v65, v110
	v_fmac_f32_e32 v87, v62, v111
	v_add_f32_e32 v86, v87, v86
	v_min_f32_e32 v87, 0, v86
	v_mul_f32_e64 v86, |v86|, s14
	v_exp_f32_e32 v86, v86
	v_fmac_f32_e32 v101, v52, v100
	v_mul_f32_e32 v97, v60, v97
	v_fmac_f32_e32 v89, v51, v88
	v_add_f32_e32 v86, 1.0, v86
	v_log_f32_e32 v86, v86
	v_mul_f32_e32 v35, v56, v35
	v_fmac_f32_e32 v101, v61, v102
	v_fmac_f32_e32 v97, v53, v96
	v_fmac_f32_e32 v87, 0xbf317218, v86
	v_fmamk_f32 v86, v87, 0x3d800000, v85
	v_mul_f32_e32 v87, v54, v105
	v_fmac_f32_e32 v87, v51, v104
	v_fmac_f32_e32 v87, v58, v106
	v_fmac_f32_e32 v87, v55, v107
	v_mul_f32_e32 v93, v64, v93
	v_fmac_f32_e32 v89, v58, v90
	v_fmac_f32_e32 v35, v52, v34
	v_mul_f32_e32 v31, v60, v31
	v_add_f32_e32 v87, v74, v87
	v_fmac_f32_e32 v101, v59, v103
	v_fmac_f32_e32 v97, v71, v98
	v_fmac_f32_e32 v93, v57, v92
	v_fmac_f32_e32 v89, v55, v91
	v_fmac_f32_e32 v35, v61, v36
	v_fmac_f32_e32 v31, v53, v30
	v_mul_f32_e32 v27, v64, v27
	v_add_f32_e32 v87, v101, v87
	v_fmac_f32_e32 v97, v63, v99
	v_fmac_f32_e32 v93, v65, v94
	v_add_f32_e32 v88, v74, v89
	v_fmac_f32_e32 v35, v59, v37
	v_fmac_f32_e32 v31, v71, v32
	v_fmac_f32_e32 v27, v57, v26
	v_add_f32_e32 v87, v97, v87
	v_fmac_f32_e32 v93, v62, v95
	v_add_f32_e32 v34, v35, v88
	v_fmac_f32_e32 v31, v63, v33
	v_fmac_f32_e32 v27, v65, v28
	v_add_f32_e32 v87, v93, v87
	v_add_f32_e32 v30, v31, v34
	v_fmac_f32_e32 v27, v62, v29
	v_min_f32_e32 v92, 0, v87
	v_mul_f32_e64 v87, |v87|, s14
	v_add_f32_e32 v26, v27, v30
	v_exp_f32_e32 v87, v87
	v_min_f32_e32 v27, 0, v26
	v_mul_f32_e64 v26, |v26|, s14
	v_exp_f32_e32 v26, v26
	v_add_f32_e32 v87, 1.0, v87
	v_log_f32_e32 v87, v87
	v_add_f32_e32 v26, 1.0, v26
	v_log_f32_e32 v26, v26
	v_fmac_f32_e32 v92, 0xbf317218, v87
	v_fmamk_f32 v87, v92, 0x3d800000, v86
	v_fmac_f32_e32 v27, 0xbf317218, v26
	v_fmamk_f32 v34, v27, 0x3d800000, v87
	ds_read_b128 v[26:29], v80 offset:1008
	ds_read_b128 v[30:33], v80 offset:992
	ds_read_b128 v[88:91], v80 offset:976
	ds_read_b128 v[92:95], v80 offset:960
	ds_read_b128 v[96:99], v80 offset:944
	ds_read_b128 v[100:103], v80 offset:928
	ds_read_b128 v[104:107], v80 offset:912
	ds_read_b128 v[108:111], v80 offset:896
	ds_read_b128 v[112:115], v80 offset:880
	ds_read_b128 v[116:119], v80 offset:864
	ds_read_b128 v[120:123], v80 offset:848
	ds_read_b128 v[124:127], v80 offset:832
	ds_read_b128 v[128:131], v80 offset:768
	ds_read_b128 v[132:135], v80 offset:784
	ds_read_b128 v[136:139], v80 offset:800
	ds_read_b128 v[140:143], v80 offset:816
	s_waitcnt lgkmcnt(0)
; #define LAS __attribute__((address_space(3)))
; __device__ __forceinline__ void gla_cum(LAS unsigned char* lds, const GlaPre pre, const float (&wa)[16], const float ba, int tid) {
;     ...
;     for (int i2 = 0; i2 < 16; i2 += 4) {
;         f32x4 bb[16];
; #pragma unroll
;         for (int e = 0; e < 16; ++e) bb[e] = *(const LAS f32x4*)(blr + (16 * q + i2 + (e >> 2)) * 16 + 4 * (e & 3));
;         asm volatile("" : "+v"(bb[0]), "+v"(bb[1]), "+v"(bb[2]), "+v"(bb[3]), "+v"(bb[4]), "+v"(bb[5]), "+v"(bb[6]), "+v"(bb[7]), "+v"(bb[8]), "+v"(bb[9]), "+v"(bb[10]), "+v"(bb[11]), "+v"(bb[12]), "+v"(bb[13]), "+v"(bb[14]), "+v"(bb[15]) :: "memory");
; #pragma unroll
;         for (int ii = 0; ii < 4; ++ii) { float x = ba;
; #pragma unroll
;             for (int j4 = 0; j4 < 4; ++j4) { const f32x4 b4 = bb[ii * 4 + j4]; x += b4.x * wa[4 * j4] + b4.y * wa[4 * j4 + 1] + b4.z * wa[4 * j4 + 2] + b4.w * wa[4 * j4 + 3]; }
;             const float ls = fminf(x, 0.f) - 0.6931471805599453f * __builtin_amdgcn_logf(1.0f + __builtin_amdgcn_exp2f(-1.4426950408889634f * fabsf(x)));
;             run += ls * (1.0f / 16.0f); c[i2 + ii] = run; } }
;     tot[q * 128 + k] = run;
;     __syncthreads();
;     float off = 0.f;
; #pragma unroll
;     for (int qq = 0; qq < 3; ++qq) off += (qq < q) ? tot[qq * 128 + k] : 0.f;
	s_nop 0
	v_mul_f32_e32 v35, v54, v129
	v_fmac_f32_e32 v35, v51, v128
	v_mul_f32_e32 v36, v56, v133
	v_fmac_f32_e32 v35, v58, v130
	v_fmac_f32_e32 v36, v52, v132
	v_fmac_f32_e32 v35, v55, v131
	v_fmac_f32_e32 v36, v61, v134
	v_add_f32_e32 v35, v74, v35
	v_fmac_f32_e32 v36, v59, v135
	v_add_f32_e32 v35, v36, v35
	v_mul_f32_e32 v36, v60, v137
	v_fmac_f32_e32 v36, v53, v136
	v_fmac_f32_e32 v36, v71, v138
	v_fmac_f32_e32 v36, v63, v139
	v_add_f32_e32 v35, v36, v35
	v_mul_f32_e32 v36, v64, v141
	v_fmac_f32_e32 v36, v57, v140
	v_fmac_f32_e32 v36, v65, v142
	v_fmac_f32_e32 v36, v62, v143
	v_add_f32_e32 v35, v36, v35
	v_min_f32_e32 v36, 0, v35
	v_mul_f32_e64 v35, |v35|, s14
	v_exp_f32_e32 v35, v35
	v_mul_f32_e32 v37, v56, v121
	v_fmac_f32_e32 v37, v52, v120
	v_fmac_f32_e32 v37, v61, v122
	v_add_f32_e32 v35, 1.0, v35
	v_log_f32_e32 v35, v35
	v_fmac_f32_e32 v37, v59, v123
	v_mul_f32_e32 v80, v56, v105
	v_fmac_f32_e32 v80, v52, v104
	v_fmac_f32_e32 v36, 0xbf317218, v35
	v_fmamk_f32 v35, v36, 0x3d800000, v34
	v_mul_f32_e32 v36, v54, v125
	v_fmac_f32_e32 v36, v51, v124
	v_fmac_f32_e32 v36, v58, v126
	v_fmac_f32_e32 v36, v55, v127
	v_add_f32_e32 v36, v74, v36
	v_add_f32_e32 v36, v37, v36
	v_mul_f32_e32 v37, v60, v117
	v_fmac_f32_e32 v37, v53, v116
	v_fmac_f32_e32 v37, v71, v118
	v_fmac_f32_e32 v37, v63, v119
	v_add_f32_e32 v36, v37, v36
	v_mul_f32_e32 v37, v64, v113
	v_fmac_f32_e32 v37, v57, v112
	v_fmac_f32_e32 v37, v65, v114
	v_fmac_f32_e32 v37, v62, v115
	v_add_f32_e32 v36, v37, v36
	v_min_f32_e32 v37, 0, v36
	v_mul_f32_e64 v36, |v36|, s14
	v_exp_f32_e32 v36, v36
	v_fmac_f32_e32 v80, v61, v106
	v_fmac_f32_e32 v80, v59, v107
	v_mul_f32_e32 v31, v60, v31
	v_add_f32_e32 v36, 1.0, v36
	v_log_f32_e32 v36, v36
	v_fmac_f32_e32 v31, v53, v30
	v_mul_f32_e32 v27, v64, v27
	v_fmac_f32_e32 v31, v71, v32
	v_fmac_f32_e32 v37, 0xbf317218, v36
	v_fmamk_f32 v36, v37, 0x3d800000, v35
	v_mul_f32_e32 v37, v54, v109
	v_fmac_f32_e32 v37, v51, v108
	v_fmac_f32_e32 v37, v58, v110
	v_fmac_f32_e32 v37, v55, v111
	v_add_f32_e32 v37, v74, v37
	v_mul_f32_e32 v54, v54, v93
	v_add_f32_e32 v37, v80, v37
	v_mul_f32_e32 v80, v60, v101
	v_fmac_f32_e32 v54, v51, v92
	v_fmac_f32_e32 v80, v53, v100
	v_fmac_f32_e32 v54, v58, v94
	v_fmac_f32_e32 v80, v71, v102
	v_fmac_f32_e32 v54, v55, v95
	v_fmac_f32_e32 v80, v63, v103
	v_add_f32_e32 v51, v74, v54
	v_mul_f32_e32 v54, v56, v89
	v_add_f32_e32 v37, v80, v37
	v_mul_f32_e32 v80, v64, v97
	v_fmac_f32_e32 v54, v52, v88
	v_fmac_f32_e32 v80, v57, v96
	v_fmac_f32_e32 v54, v61, v90
	v_fmac_f32_e32 v80, v65, v98
	v_fmac_f32_e32 v54, v59, v91
	v_fmac_f32_e32 v27, v57, v26
	v_fmac_f32_e32 v80, v62, v99
	v_add_f32_e32 v51, v54, v51
	v_fmac_f32_e32 v31, v63, v33
	v_fmac_f32_e32 v27, v65, v28
	v_add_f32_e32 v37, v80, v37
	v_add_f32_e32 v30, v31, v51
	v_fmac_f32_e32 v27, v62, v29
	v_min_f32_e32 v80, 0, v37
	v_mul_f32_e64 v37, |v37|, s14
	v_add_f32_e32 v26, v27, v30
	v_exp_f32_e32 v37, v37
	v_min_f32_e32 v27, 0, v26
	v_mul_f32_e64 v26, |v26|, s14
	v_exp_f32_e32 v26, v26
	v_add_f32_e32 v37, 1.0, v37
	v_log_f32_e32 v37, v37
	v_readlane_b32 s14, v254, 45
	v_add_f32_e32 v26, 1.0, v26
	v_log_f32_e32 v26, v26
	v_fmac_f32_e32 v80, 0xbf317218, v37
	v_fmamk_f32 v37, v80, 0x3d800000, v36
	v_add_u32_e32 v28, s14, v49
	v_fmac_f32_e32 v27, 0xbf317218, v26
	v_fmamk_f32 v26, v27, 0x3d800000, v37
	v_and_b32_e32 v27, 0x7f, v70
	ds_write_b32 v28, v26
	v_lshl_add_u32 v29, v27, 2, s14
	v_mov_b32_e32 v28, 0
	s_waitcnt lgkmcnt(0)
	s_barrier
	s_and_saveexec_b64 s[14:15], vcc
	s_cbranch_execz .LBB0_918
	ds_read_b32 v28, v29
	s_waitcnt lgkmcnt(0)
	v_add_f32_e32 v28, 0, v28

; #define INP(k) ldptr(PTAB, (k))
; __global__ void __launch_bounds__(NWAVES * 64, 2) fwd_kernel(Args args) {
;     ...
;             { BODY_LOCALS
;               for (int it = vcu; it < 1024; it += G) { float wa[16], ba; gla_alpha_load(wa, ba, INP(6) + (size_t)l * 16 * 512, INP(7) + l * 512, (it >> 6) & 3, tid);
;                   const GlaPre cur = gla_blr_load(WSP(WS_ZABC), (size_t)(it >> 8) * SEQ + 64 * (it & 63), tid);
;                   gla_g3(ring, WSP(WS_ZABC), ((bf16*)xo), WSP(WS_OABC), cur, wa, ba, INP(8) + l * 1024, it, tid); } }
.LBB0_1110:
	s_or_b64 exec, exec, s[38:39]
	v_readlane_b32 s8, v252, 6
	v_readlane_b32 s4, v252, 4
	v_readlane_b32 s14, v252, 12
	v_readlane_b32 s15, v252, 13
	v_readlane_b32 s0, v252, 32
	v_readlane_b32 s5, v252, 5
	s_mov_b64 s[6:7], s[14:15]
	v_readlane_b32 s1, v252, 33
	s_waitcnt lgkmcnt(0)
	s_barrier
	v_mbcnt_lo_u32_b32 v0, -1, 0
	v_mbcnt_hi_u32_b32 v0, -1, v0
	s_and_b64 vcc, exec, s[0:1]
	v_readlane_b32 s9, v252, 7
	v_readlane_b32 s10, v252, 8
	v_readlane_b32 s11, v252, 9
	v_readlane_b32 s12, v252, 10
	v_readlane_b32 s13, v252, 11
	v_mbcnt_lo_u32_b32 v0, -1, 0
	v_mbcnt_hi_u32_b32 v0, -1, v0
	s_cbranch_vccz .LBB0_1119
	v_readlane_b32 s0, v255, 23
	s_lshl_b32 s94, s0, 10
	s_add_u32 s8, s4, 0x15600000
	v_readlane_b32 s0, v252, 37
	s_addc_u32 s9, s5, 0
	v_readlane_b32 s1, v255, 24
	v_add_u32_e32 v136, s0, v0
	s_add_u32 s0, s4, 0x29e00000
	v_ashrrev_i32_e32 v130, 4, v136
	v_and_b32_e32 v0, 15, v0
	s_addc_u32 s1, s5, 0
	v_readlane_b32 s12, v254, 8
	v_readlane_b32 s4, v254, 12
	v_and_b32_e32 v137, 0x7f, v136
	v_ashrrev_i32_e32 v131, 31, v130
	v_lshlrev_b32_e32 v132, 1, v0
	s_lshl_b64 s[10:11], s[94:95], 2
	v_readlane_b32 s13, v254, 9
	v_readlane_b32 s16, v253, 58
	s_mov_b32 s17, s4
	v_readlane_b32 s5, v254, 13
	s_mov_b32 s32, 0
	s_branch .LBB0_1113

; __device__ __forceinline__ void gla_alpha_load(float (&wa)[16], float& ba, const float* w_alpha, const float* b_alpha, int h, int tid) {
;     const int k = tid & 127;
; #pragma unroll
;     for (int j = 0; j < 16; ++j) wa[j] = w_alpha[j * 512 + h * 128 + k];
;     ba = b_alpha[h * 128 + k];
; }
.LBB0_1113:
	v_readlane_b32 s4, v254, 43
	v_mov_b64_e32 v[14:15], s[8:9]
	s_movk_i32 s21, 0x2200
	v_mov_b32_e32 v0, s4
	ds_read_b64 v[2:3], v0
	s_lshl_b64 s[4:5], s[50:51], 2
	v_mov_b32_e32 v133, v1
	v_mov_b32_e32 v17, v1
	s_waitcnt lgkmcnt(0)
	v_readfirstlane_b32 s15, v2
	v_readfirstlane_b32 s14, v3
	s_add_u32 s4, s15, s4
	s_addc_u32 s5, s14, s5
	v_readlane_b32 s14, v254, 44
	s_nop 1
	v_mov_b32_e32 v0, s14
	ds_read_b64 v[2:3], v0
	v_readlane_b32 s14, v255, 31
	v_readlane_b32 s15, v255, 32
	s_lshl_b64 s[14:15], s[14:15], 2
	s_waitcnt lgkmcnt(0)
	v_readfirstlane_b32 s18, v2
	v_readfirstlane_b32 s19, v3
	s_add_u32 s18, s18, s14
	s_addc_u32 s19, s19, s15
	s_bfe_u32 s15, s17, 0x20006
	s_lshl_b32 s14, s15, 9
	s_cmp_eq_u32 s32, 0
	s_cselect_b64 exec, -1, 0
	v_lshl_or_b32 v0, v137, 2, s14
	v_lshl_add_u64 v[2:3], s[4:5], 0, v[0:1]
	v_add_co_u32_e32 v4, vcc, s43, v2
	global_load_dword v59, v0, s[4:5]
	global_load_dword v62, v0, s[4:5] offset:2048
	v_addc_co_u32_e32 v5, vcc, 0, v3, vcc
	v_add_co_u32_e32 v6, vcc, s84, v2
	s_movk_i32 s4, 0x4000
	s_nop 0
	v_addc_co_u32_e32 v7, vcc, 0, v3, vcc
	global_load_dword v66, v[6:7], off offset:-4096
	global_load_dword v63, v[4:5], off offset:2048
	global_load_dword v60, v[6:7], off
	global_load_dword v64, v[6:7], off offset:2048
	v_add_co_u32_e32 v4, vcc, s37, v2
	s_lshl_b32 s94, s15, 8
	s_nop 0
	v_addc_co_u32_e32 v5, vcc, 0, v3, vcc
	v_add_co_u32_e32 v6, vcc, s4, v2
	s_movk_i32 s4, 0x5000
	s_nop 0
	v_addc_co_u32_e32 v7, vcc, 0, v3, vcc
	global_load_dword v69, v[6:7], off offset:-4096
	global_load_dword v67, v[4:5], off offset:2048
	global_load_dword v61, v[6:7], off
	global_load_dword v68, v[6:7], off offset:2048
	v_add_co_u32_e32 v4, vcc, s4, v2
	s_movk_i32 s4, 0x6000
	s_nop 0
	v_addc_co_u32_e32 v5, vcc, 0, v3, vcc
	v_add_co_u32_e32 v6, vcc, s4, v2
	s_movk_i32 s4, 0x7000
	s_nop 0
	v_addc_co_u32_e32 v7, vcc, 0, v3, vcc
	v_add_co_u32_e32 v2, vcc, s4, v2
	s_ashr_i32 s4, s17, 8
	s_nop 0
	v_addc_co_u32_e32 v3, vcc, 0, v3, vcc
	s_ashr_i32 s5, s4, 31
	global_load_dword v74, v[6:7], off offset:-4096
	global_load_dword v71, v[4:5], off offset:2048
	global_load_dword v65, v[6:7], off
	global_load_dword v72, v[6:7], off offset:2048
	global_load_dword v73, v[2:3], off
	global_load_dword v70, v[2:3], off offset:2048
	global_load_dword v75, v0, s[18:19]
	s_mov_b64 exec, -1
	s_lshl_b64 s[4:5], s[4:5], 12
	s_and_b32 s18, s16, 0xfc0
	s_or_b32 s4, s4, s18
	v_lshl_add_u64 v[2:3], s[4:5], 0, v[130:131]
	v_mad_u64_u32 v[4:5], s[18:19], v2, s21, v[14:15]
	v_mad_i32_i24 v5, v3, s21, v5
	v_lshl_add_u64 v[2:3], v[4:5], 0, v[132:133]
	s_mov_b32 s18, 0x46000
	v_add_co_u32_e32 v4, vcc, s18, v2
	v_readlane_b32 s18, v255, 14
	s_nop 0
	v_addc_co_u32_e32 v5, vcc, 0, v3, vcc
	s_cmp_eq_u32 s32, 0
	s_cselect_b64 exec, -1, 0
	global_load_ushort v0, v[4:5], off offset:128
	s_mov_b64 exec, -1
	v_add_co_u32_e32 v2, vcc, s84, v2
	v_mov_b32_e32 v133, v136
	s_nop 0
	v_addc_co_u32_e32 v3, vcc, 0, v3, vcc
	s_cmp_eq_u32 s32, 0
	s_cselect_b64 exec, -1, 0
	global_load_ushort v37, v[2:3], off offset:128
	s_mov_b64 exec, -1
	s_mov_b32 s15, s95
	s_cmp_eq_u32 s32, 0
	s_cbranch_scc1 .Lg3_first
	v_mov_b32_e32 v0, v197
	v_mov_b32_e32 v37, v198
	v_mov_b32_e32 v59, v180
	v_mov_b32_e32 v62, v181
	v_mov_b32_e32 v66, v182
	v_mov_b32_e32 v63, v183
	v_mov_b32_e32 v60, v184
	v_mov_b32_e32 v64, v185
	v_mov_b32_e32 v69, v186
	v_mov_b32_e32 v67, v187
	v_mov_b32_e32 v61, v188
	v_mov_b32_e32 v68, v189
	v_mov_b32_e32 v74, v190
	v_mov_b32_e32 v71, v191
	v_mov_b32_e32 v65, v192
	v_mov_b32_e32 v72, v193
	v_mov_b32_e32 v73, v194
	v_mov_b32_e32 v70, v195
	v_mov_b32_e32 v75, v196
	s_branch .Lg3_pf
.Lg3_first:
	s_waitcnt vmcnt(0)
	v_mov_b32_e32 v180, v59
	v_mov_b32_e32 v181, v62
	v_mov_b32_e32 v182, v66
	v_mov_b32_e32 v183, v63
	v_mov_b32_e32 v184, v60
	v_mov_b32_e32 v185, v64
	v_mov_b32_e32 v186, v69
	v_mov_b32_e32 v187, v67
	v_mov_b32_e32 v188, v61
	v_mov_b32_e32 v189, v68
	v_mov_b32_e32 v190, v74
	v_mov_b32_e32 v191, v71
	v_mov_b32_e32 v192, v65
	v_mov_b32_e32 v193, v72
	v_mov_b32_e32 v194, v73
	v_mov_b32_e32 v195, v70
	v_mov_b32_e32 v196, v75
	s_mov_b32 s32, 1
.Lg3_pf:
	s_add_i32 s98, s17, s78
	s_cmpk_gt_i32 s98, 0x3ff
	s_cbranch_scc1 .Lg3_join
	s_mov_b64 s[98:99], 0x2200000
	v_lshl_add_u64 v[200:201], v[4:5], 0, s[98:99]
	global_load_ushort v197, v[200:201], off offset:128
	v_lshl_add_u64 v[200:201], v[2:3], 0, s[98:99]
	global_load_ushort v198, v[200:201], off offset:128
; #define LAS __attribute__((address_space(3)))
; __device__ __forceinline__ void gla_cum(LAS unsigned char* lds, const GlaPre pre, const float (&wa)[16], const float ba, int tid) {
;     LAS float* cum = (LAS float*)(lds + GL_CUM); LAS float* blr = (LAS float*)(lds + GL_BLR); LAS float* tot = blr + 1024;
;     blr[tid] = __uint_as_float((unsigned)pre.b0 << 16); blr[tid + 512] = __uint_as_float((unsigned)pre.b1 << 16);
;     const int k = tid & 127, q = tid >> 7;
;     __syncthreads();
;     float c[16]; float run = 0.f;
; #pragma unroll
;     for (int i2 = 0; i2 < 16; i2 += 4) {
;         f32x4 bb[16];
; #pragma unroll
;         for (int e = 0; e < 16; ++e) bb[e] = *(const LAS f32x4*)(blr + (16 * q + i2 + (e >> 2)) * 16 + 4 * (e & 3));
;         asm volatile("" : "+v"(bb[0]), "+v"(bb[1]), "+v"(bb[2]), "+v"(bb[3]), "+v"(bb[4]), "+v"(bb[5]), "+v"(bb[6]), "+v"(bb[7]), "+v"(bb[8]), "+v"(bb[9]), "+v"(bb[10]), "+v"(bb[11]), "+v"(bb[12]), "+v"(bb[13]), "+v"(bb[14]), "+v"(bb[15]) :: "memory");
; #pragma unroll
;         for (int ii = 0; ii < 4; ++ii) { float x = ba;
; #pragma unroll
;             for (int j4 = 0; j4 < 4; ++j4) { const f32x4 b4 = bb[ii * 4 + j4]; x += b4.x * wa[4 * j4] + b4.y * wa[4 * j4 + 1] + b4.z * wa[4 * j4 + 2] + b4.w * wa[4 * j4 + 3]; }
;             const float ls = fminf(x, 0.f) - 0.6931471805599453f * __builtin_amdgcn_logf(1.0f + __builtin_amdgcn_exp2f(-1.4426950408889634f * fabsf(x)));
;             run += ls * (1.0f / 16.0f); c[i2 + ii] = run; } }
; __device__ __forceinline__ void gla_g3(LAS unsigned char* lds, const bf16* Z, const bf16* ST, bf16* Oabc, const GlaPre pre, const float (&wa)[16], const float ba, const float* gla_norm, int item, int tid) {
;     using namespace fa;
;     asm volatile("" : "+v"(tid));
;     const int wid = __builtin_amdgcn_readfirstlane(tid >> 6), lane = tid & 63, r32 = lane & 31, hf = lane >> 5;
;     const int bh = item >> 6, n = item & 63, b = bh >> 2, h = bh & 3; const size_t m0 = (size_t)b * SEQ + 64 * n;
;     v4u qraw[2], kraw[2];
; #pragma unroll
;     for (int i = 0; i < 2; ++i) { const int t = (tid >> 4) + 32 * i, kc = (tid & 15) * 8;
;         qraw[i] = *(const v4u*)(Z + (m0 + t) * NABC + ZC_BQ + h * 128 + kc); kraw[i] = *(const v4u*)(Z + (m0 + t) * NABC + ZC_BK + h * 128 + kc); }
;     const GlaV vraw = gla_load_v(Z, m0, h, tid);
;     gla_cum(lds, pre, wa, ba, tid);
.Lg3_join:
	v_lshlrev_b32_e32 v36, 16, v0
	v_mov_b32_e32 v0, s18
	ds_read_b64 v[2:3], v0
	s_waitcnt lgkmcnt(0)
	v_readfirstlane_b32 s19, v3
	v_ashrrev_i32_e32 v56, 4, v133
	v_ashrrev_i32_e32 v57, 31, v56
	v_readfirstlane_b32 s20, v2
	v_lshl_add_u64 v[2:3], s[4:5], 0, v[56:57]
	v_lshlrev_b32_e32 v0, 3, v133
	v_mad_u64_u32 v[4:5], s[22:23], v2, s21, v[14:15]
	v_and_b32_e32 v58, 0x78, v0
	v_mad_i32_i24 v5, v3, s21, v5
	v_lshl_add_u64 v[2:3], v[4:5], 0, s[94:95]
	v_lshlrev_b32_e32 v0, 1, v58
	v_add_u32_e32 v48, 32, v56
	v_lshl_add_u64 v[2:3], v[2:3], 0, v[0:1]
	v_ashrrev_i32_e32 v49, 31, v48
	global_load_dwordx4 v[30:33], v[2:3], off
	global_load_dwordx4 v[26:29], v[2:3], off offset:1024
	v_lshl_add_u64 v[2:3], s[4:5], 0, v[48:49]
	v_add_u32_e32 v49, 0x200, v133
	v_ashrrev_i32_e32 v50, 5, v49
	v_ashrrev_i32_e32 v51, 31, v50
	v_lshl_add_u64 v[6:7], s[4:5], 0, v[50:51]
	v_add_u32_e32 v51, 0x400, v133
	v_ashrrev_i32_e32 v52, 5, v51
	v_mad_u64_u32 v[4:5], s[22:23], v2, s21, v[14:15]
	v_ashrrev_i32_e32 v53, 31, v52
	v_mad_i32_i24 v5, v3, s21, v5
	v_lshl_add_u64 v[10:11], s[4:5], 0, v[52:53]
	v_add_u32_e32 v53, 0x600, v133
	v_lshl_add_u64 v[2:3], v[4:5], 0, s[94:95]
	v_ashrrev_i32_e32 v46, 5, v133
	v_ashrrev_i32_e32 v54, 5, v53
	v_lshl_add_u64 v[2:3], v[2:3], 0, v[0:1]
	v_ashrrev_i32_e32 v47, 31, v46
	v_ashrrev_i32_e32 v55, 31, v54
	global_load_dwordx4 v[22:25], v[2:3], off
	global_load_dwordx4 v[18:21], v[2:3], off offset:1024
	v_lshl_add_u64 v[2:3], s[4:5], 0, v[46:47]
	v_lshl_add_u64 v[34:35], s[4:5], 0, v[54:55]
	v_mad_u64_u32 v[4:5], s[22:23], v2, s21, v[14:15]
	v_mad_u64_u32 v[8:9], s[22:23], v6, s21, v[14:15]
	v_mad_u64_u32 v[12:13], s[22:23], v10, s21, v[14:15]
	v_mad_u64_u32 v[14:15], s[22:23], v34, s21, v[14:15]
	v_mad_i32_i24 v5, v3, s21, v5
	v_lshlrev_b32_e32 v47, 4, v133
	v_mad_i32_i24 v9, v7, s21, v9
	v_mad_i32_i24 v13, v11, s21, v13
	v_mad_i32_i24 v15, v35, s21, v15
	v_lshl_add_u64 v[2:3], v[4:5], 0, s[14:15]
	v_and_b32_e32 v16, 0x1f0, v47
	v_lshl_add_u64 v[6:7], v[8:9], 0, s[14:15]
	v_lshl_add_u64 v[10:11], v[12:13], 0, s[14:15]
	v_lshl_add_u64 v[14:15], v[14:15], 0, s[14:15]
	s_add_i32 s14, 0, 0x18000
	v_lshlrev_b32_e32 v57, 2, v133
	v_ashrrev_i32_e32 v55, 7, v133
	v_lshl_add_u64 v[2:3], v[2:3], 0, v[16:17]
	v_lshl_add_u64 v[6:7], v[6:7], 0, v[16:17]
	v_lshl_add_u64 v[10:11], v[10:11], 0, v[16:17]
	v_lshl_add_u64 v[14:15], v[14:15], 0, v[16:17]
	v_lshlrev_b32_e32 v34, 16, v37
	v_add_u32_e32 v35, s14, v57
	v_lshl_add_u32 v81, v55, 10, s14
	global_load_dwordx4 v[2:5], v[2:3], off offset:2048
	ds_write2st64_b32 v35, v34, v36 offset1:8
	global_load_dwordx4 v[6:9], v[6:7], off offset:2048
	s_mov_b32 s14, 0xbfb8aa3b
	global_load_dwordx4 v[10:13], v[10:11], off offset:2048
	s_mov_b32 s15, 0x3d800000
	global_load_dwordx4 v[14:17], v[14:15], off offset:2048
	s_waitcnt lgkmcnt(0)
	s_barrier
	ds_read_b128 v[34:37], v81 offset:240
	ds_read_b128 v[38:41], v81 offset:224
	ds_read_b128 v[42:45], v81 offset:208
	ds_read_b128 v[82:85], v81 offset:192
	ds_read_b128 v[86:89], v81 offset:176
	ds_read_b128 v[90:93], v81 offset:160
	ds_read_b128 v[94:97], v81 offset:144
	ds_read_b128 v[98:101], v81 offset:128
	ds_read_b128 v[102:105], v81 offset:112
	ds_read_b128 v[106:109], v81 offset:96
	ds_read_b128 v[110:113], v81 offset:80
	ds_read_b128 v[114:117], v81 offset:64
	ds_read_b128 v[76:79], v81
	ds_read_b128 v[118:121], v81 offset:16
	ds_read_b128 v[122:125], v81 offset:32
	ds_read_b128 v[126:129], v81 offset:48
	s_waitcnt lgkmcnt(0)
	s_nop 0
	v_mul_f32_e32 v77, v62, v77
	v_fmac_f32_e32 v77, v59, v76
	v_fmac_f32_e32 v77, v66, v78
	v_fmac_f32_e32 v77, v63, v79
	v_add_f32_e32 v76, v75, v77
	v_mul_f32_e32 v77, v64, v119
	v_fmac_f32_e32 v77, v60, v118
	v_fmac_f32_e32 v77, v69, v120
	v_fmac_f32_e32 v77, v67, v121
	v_add_f32_e32 v76, v77, v76
	v_mul_f32_e32 v77, v68, v123
	v_fmac_f32_e32 v77, v61, v122
	v_fmac_f32_e32 v77, v74, v124
	v_fmac_f32_e32 v77, v71, v125
	v_add_f32_e32 v76, v77, v76
	v_mul_f32_e32 v77, v72, v127
	v_fmac_f32_e32 v77, v65, v126
	v_fmac_f32_e32 v77, v73, v128
	v_fmac_f32_e32 v77, v70, v129
	v_add_f32_e32 v77, v77, v76
	v_min_f32_e32 v78, 0, v77
	v_mul_f32_e64 v77, |v77|, s14
	v_exp_f32_e32 v77, v77
	v_mul_f32_e32 v79, v64, v111
	v_fmac_f32_e32 v79, v60, v110
	v_fmac_f32_e32 v79, v69, v112
	v_add_f32_e32 v77, 1.0, v77
	v_log_f32_e32 v77, v77
	v_fmac_f32_e32 v79, v67, v113
	v_mul_f32_e32 v80, v64, v95
	v_fmac_f32_e32 v80, v60, v94
	v_fmac_f32_e32 v78, 0xbf317218, v77
	v_fma_f32 v77, v78, s15, 0
	v_mul_f32_e32 v78, v62, v115
	v_fmac_f32_e32 v78, v59, v114
	v_fmac_f32_e32 v78, v66, v116
	v_fmac_f32_e32 v78, v63, v117
	v_add_f32_e32 v78, v75, v78
	v_add_f32_e32 v78, v79, v78
	v_mul_f32_e32 v79, v68, v107
	v_fmac_f32_e32 v79, v61, v106
	v_fmac_f32_e32 v79, v74, v108
	v_fmac_f32_e32 v79, v71, v109
	v_add_f32_e32 v78, v79, v78
	v_mul_f32_e32 v79, v72, v103
	v_fmac_f32_e32 v79, v65, v102
	v_fmac_f32_e32 v79, v73, v104
	v_fmac_f32_e32 v79, v70, v105
	v_add_f32_e32 v78, v79, v78
	v_min_f32_e32 v79, 0, v78
	v_mul_f32_e64 v78, |v78|, s14
	v_exp_f32_e32 v78, v78
	v_fmac_f32_e32 v80, v69, v96
	v_fmac_f32_e32 v80, v67, v97
	v_mul_f32_e32 v43, v64, v43
	v_add_f32_e32 v78, 1.0, v78
	v_log_f32_e32 v78, v78
	v_fmac_f32_e32 v43, v60, v42
	v_mul_f32_e32 v39, v68, v39
	v_fmac_f32_e32 v43, v69, v44
	v_fmac_f32_e32 v79, 0xbf317218, v78
	v_fmamk_f32 v78, v79, 0x3d800000, v77
	v_mul_f32_e32 v79, v62, v99
	v_fmac_f32_e32 v79, v59, v98
	v_fmac_f32_e32 v79, v66, v100
	v_fmac_f32_e32 v79, v63, v101
	v_add_f32_e32 v79, v75, v79
	v_add_f32_e32 v79, v80, v79
	v_mul_f32_e32 v80, v68, v91
	v_fmac_f32_e32 v80, v61, v90
	v_fmac_f32_e32 v80, v74, v92
	v_fmac_f32_e32 v80, v71, v93
; #define LAS __attribute__((address_space(3)))
; __device__ __forceinline__ void gla_cum(LAS unsigned char* lds, const GlaPre pre, const float (&wa)[16], const float ba, int tid) {
;     ...
;     for (int i2 = 0; i2 < 16; i2 += 4) {
;         f32x4 bb[16];
; #pragma unroll
;         for (int e = 0; e < 16; ++e) bb[e] = *(const LAS f32x4*)(blr + (16 * q + i2 + (e >> 2)) * 16 + 4 * (e & 3));
;         asm volatile("" : "+v"(bb[0]), "+v"(bb[1]), "+v"(bb[2]), "+v"(bb[3]), "+v"(bb[4]), "+v"(bb[5]), "+v"(bb[6]), "+v"(bb[7]), "+v"(bb[8]), "+v"(bb[9]), "+v"(bb[10]), "+v"(bb[11]), "+v"(bb[12]), "+v"(bb[13]), "+v"(bb[14]), "+v"(bb[15]) :: "memory");
; #pragma unroll
;         for (int ii = 0; ii < 4; ++ii) { float x = ba;
; #pragma unroll
;             for (int j4 = 0; j4 < 4; ++j4) { const f32x4 b4 = bb[ii * 4 + j4]; x += b4.x * wa[4 * j4] + b4.y * wa[4 * j4 + 1] + b4.z * wa[4 * j4 + 2] + b4.w * wa[4 * j4 + 3]; }
;             const float ls = fminf(x, 0.f) - 0.6931471805599453f * __builtin_amdgcn_logf(1.0f + __builtin_amdgcn_exp2f(-1.4426950408889634f * fabsf(x)));
;             run += ls * (1.0f / 16.0f); c[i2 + ii] = run; } }
	v_add_f32_e32 v79, v80, v79
	v_mul_f32_e32 v80, v72, v87
	v_fmac_f32_e32 v80, v65, v86
	v_fmac_f32_e32 v80, v73, v88
	v_fmac_f32_e32 v80, v70, v89
	v_add_f32_e32 v79, v80, v79
	v_min_f32_e32 v80, 0, v79
	v_mul_f32_e64 v79, |v79|, s14
	v_exp_f32_e32 v79, v79
	v_fmac_f32_e32 v39, v61, v38
	v_mul_f32_e32 v35, v72, v35
	v_fmac_f32_e32 v43, v67, v45
	v_add_f32_e32 v79, 1.0, v79
	v_log_f32_e32 v79, v79
	v_fmac_f32_e32 v39, v74, v40
	v_fmac_f32_e32 v35, v65, v34
	v_fmac_f32_e32 v39, v71, v41
	v_fmac_f32_e32 v80, 0xbf317218, v79
	v_fmamk_f32 v79, v80, 0x3d800000, v78
	v_mul_f32_e32 v80, v62, v83
	v_fmac_f32_e32 v80, v59, v82
	v_fmac_f32_e32 v80, v66, v84
	v_fmac_f32_e32 v80, v63, v85
	v_add_f32_e32 v80, v75, v80
	v_add_f32_e32 v42, v43, v80
	v_fmac_f32_e32 v35, v73, v36
	v_add_f32_e32 v38, v39, v42
	v_fmac_f32_e32 v35, v70, v37
	v_add_f32_e32 v34, v35, v38
	v_min_f32_e32 v35, 0, v34
	v_mul_f32_e64 v34, |v34|, s14
	v_exp_f32_e32 v34, v34
	v_readfirstlane_b32 s18, v133
	v_mov_b32_e32 v76, 0
	v_cmp_lt_i32_e32 vcc, 0, v55
	v_add_f32_e32 v34, 1.0, v34
	v_log_f32_e32 v34, v34
	s_nop 0
	v_fmac_f32_e32 v35, 0xbf317218, v34
	v_fmamk_f32 v80, v35, 0x3d800000, v79
	ds_read_b128 v[34:37], v81 offset:496
	ds_read_b128 v[38:41], v81 offset:480
	ds_read_b128 v[42:45], v81 offset:464
	ds_read_b128 v[86:89], v81 offset:448
	ds_read_b128 v[90:93], v81 offset:432
	ds_read_b128 v[94:97], v81 offset:416
	ds_read_b128 v[98:101], v81 offset:400
	ds_read_b128 v[102:105], v81 offset:384
	ds_read_b128 v[106:109], v81 offset:368
	ds_read_b128 v[110:113], v81 offset:352
	ds_read_b128 v[114:117], v81 offset:336
	ds_read_b128 v[118:121], v81 offset:320
	ds_read_b128 v[82:85], v81 offset:256
	ds_read_b128 v[122:125], v81 offset:272
	ds_read_b128 v[126:129], v81 offset:288
	ds_read_b128 v[138:141], v81 offset:304
	s_waitcnt lgkmcnt(0)
	s_nop 0
	v_mul_f32_e32 v83, v62, v83
	v_fmac_f32_e32 v83, v59, v82
	v_fmac_f32_e32 v83, v66, v84
	v_fmac_f32_e32 v83, v63, v85
	v_add_f32_e32 v82, v75, v83
	v_mul_f32_e32 v83, v64, v123
	v_fmac_f32_e32 v83, v60, v122
	v_fmac_f32_e32 v83, v69, v124
	v_fmac_f32_e32 v83, v67, v125
	v_add_f32_e32 v82, v83, v82
	v_mul_f32_e32 v83, v68, v127
	v_fmac_f32_e32 v83, v61, v126
	v_fmac_f32_e32 v83, v74, v128
	v_fmac_f32_e32 v83, v71, v129
	v_add_f32_e32 v82, v83, v82
	v_mul_f32_e32 v83, v72, v139
	v_fmac_f32_e32 v83, v65, v138
	v_fmac_f32_e32 v83, v73, v140
	v_fmac_f32_e32 v83, v70, v141
	v_add_f32_e32 v82, v83, v82
	v_min_f32_e32 v83, 0, v82
	v_mul_f32_e64 v82, |v82|, s14
	v_exp_f32_e32 v82, v82
	v_mul_f32_e32 v84, v64, v115
	v_fmac_f32_e32 v84, v60, v114
	v_fmac_f32_e32 v84, v69, v116
	v_add_f32_e32 v82, 1.0, v82
	v_log_f32_e32 v82, v82
	v_fmac_f32_e32 v84, v67, v117
	v_mul_f32_e32 v85, v64, v99
	v_fmac_f32_e32 v85, v60, v98
	v_fmac_f32_e32 v83, 0xbf317218, v82
	v_fmamk_f32 v82, v83, 0x3d800000, v80
	v_mul_f32_e32 v83, v62, v119
	v_fmac_f32_e32 v83, v59, v118
	v_fmac_f32_e32 v83, v66, v120
	v_fmac_f32_e32 v83, v63, v121
	v_add_f32_e32 v83, v75, v83
	v_add_f32_e32 v83, v84, v83
	v_mul_f32_e32 v84, v68, v111
	v_fmac_f32_e32 v84, v61, v110
	v_fmac_f32_e32 v84, v74, v112
	v_fmac_f32_e32 v84, v71, v113
	v_add_f32_e32 v83, v84, v83
	v_mul_f32_e32 v84, v72, v107
	v_fmac_f32_e32 v84, v65, v106
	v_fmac_f32_e32 v84, v73, v108
	v_fmac_f32_e32 v84, v70, v109
	v_add_f32_e32 v83, v84, v83
	v_min_f32_e32 v84, 0, v83
	v_mul_f32_e64 v83, |v83|, s14
	v_exp_f32_e32 v83, v83
	v_fmac_f32_e32 v85, v69, v100
	v_fmac_f32_e32 v85, v67, v101
	v_mul_f32_e32 v43, v64, v43
	v_add_f32_e32 v83, 1.0, v83
	v_log_f32_e32 v83, v83
	v_fmac_f32_e32 v43, v60, v42
	v_mul_f32_e32 v39, v68, v39
	v_fmac_f32_e32 v43, v69, v44
	v_fmac_f32_e32 v84, 0xbf317218, v83
	v_fmamk_f32 v83, v84, 0x3d800000, v82
	v_mul_f32_e32 v84, v62, v103
	v_fmac_f32_e32 v84, v59, v102
	v_fmac_f32_e32 v84, v66, v104
	v_fmac_f32_e32 v84, v63, v105
	v_add_f32_e32 v84, v75, v84
	v_add_f32_e32 v84, v85, v84
	v_mul_f32_e32 v85, v68, v95
	v_fmac_f32_e32 v85, v61, v94
	v_fmac_f32_e32 v85, v74, v96
	v_fmac_f32_e32 v85, v71, v97
	v_add_f32_e32 v84, v85, v84
	v_mul_f32_e32 v85, v72, v91
	v_fmac_f32_e32 v85, v65, v90
	v_fmac_f32_e32 v85, v73, v92
	v_fmac_f32_e32 v85, v70, v93
	v_add_f32_e32 v84, v85, v84
	v_min_f32_e32 v85, 0, v84
	v_mul_f32_e64 v84, |v84|, s14
	v_exp_f32_e32 v84, v84
	v_fmac_f32_e32 v39, v61, v38
	v_mul_f32_e32 v35, v72, v35
	v_fmac_f32_e32 v43, v67, v45
	v_add_f32_e32 v84, 1.0, v84
	v_log_f32_e32 v84, v84
	v_fmac_f32_e32 v39, v74, v40
	v_fmac_f32_e32 v35, v65, v34
	v_fmac_f32_e32 v39, v71, v41
	v_fmac_f32_e32 v85, 0xbf317218, v84
	v_fmamk_f32 v84, v85, 0x3d800000, v83
	v_mul_f32_e32 v85, v62, v87
	v_fmac_f32_e32 v85, v59, v86
	v_fmac_f32_e32 v85, v66, v88
	v_fmac_f32_e32 v85, v63, v89
	v_add_f32_e32 v85, v75, v85
	v_add_f32_e32 v42, v43, v85
	v_fmac_f32_e32 v35, v73, v36
	v_add_f32_e32 v38, v39, v42
	v_fmac_f32_e32 v35, v70, v37
	v_add_f32_e32 v34, v35, v38
	v_min_f32_e32 v35, 0, v34
	v_mul_f32_e64 v34, |v34|, s14
	v_exp_f32_e32 v34, v34
	s_nop 0
	v_add_f32_e32 v34, 1.0, v34
	v_log_f32_e32 v34, v34
	s_nop 0
	v_fmac_f32_e32 v35, 0xbf317218, v34
	v_fmamk_f32 v85, v35, 0x3d800000, v84
	ds_read_b128 v[34:37], v81 offset:752
	ds_read_b128 v[38:41], v81 offset:736
	ds_read_b128 v[42:45], v81 offset:720
	ds_read_b128 v[90:93], v81 offset:704
	ds_read_b128 v[94:97], v81 offset:688
	ds_read_b128 v[98:101], v81 offset:672
	ds_read_b128 v[102:105], v81 offset:656
	ds_read_b128 v[106:109], v81 offset:640
	ds_read_b128 v[110:113], v81 offset:624
	ds_read_b128 v[114:117], v81 offset:608
	ds_read_b128 v[118:121], v81 offset:592
	ds_read_b128 v[122:125], v81 offset:576
	ds_read_b128 v[86:89], v81 offset:512
	ds_read_b128 v[126:129], v81 offset:528
	ds_read_b128 v[138:141], v81 offset:544
	ds_read_b128 v[142:145], v81 offset:560
	s_waitcnt lgkmcnt(0)
; #define LAS __attribute__((address_space(3)))
; __device__ __forceinline__ void gla_cum(LAS unsigned char* lds, const GlaPre pre, const float (&wa)[16], const float ba, int tid) {
;     ...
;     for (int i2 = 0; i2 < 16; i2 += 4) {
;         f32x4 bb[16];
; #pragma unroll
;         for (int e = 0; e < 16; ++e) bb[e] = *(const LAS f32x4*)(blr + (16 * q + i2 + (e >> 2)) * 16 + 4 * (e & 3));
;         asm volatile("" : "+v"(bb[0]), "+v"(bb[1]), "+v"(bb[2]), "+v"(bb[3]), "+v"(bb[4]), "+v"(bb[5]), "+v"(bb[6]), "+v"(bb[7]), "+v"(bb[8]), "+v"(bb[9]), "+v"(bb[10]), "+v"(bb[11]), "+v"(bb[12]), "+v"(bb[13]), "+v"(bb[14]), "+v"(bb[15]) :: "memory");
; #pragma unroll
;         for (int ii = 0; ii < 4; ++ii) { float x = ba;
; #pragma unroll
;             for (int j4 = 0; j4 < 4; ++j4) { const f32x4 b4 = bb[ii * 4 + j4]; x += b4.x * wa[4 * j4] + b4.y * wa[4 * j4 + 1] + b4.z * wa[4 * j4 + 2] + b4.w * wa[4 * j4 + 3]; }
;             const float ls = fminf(x, 0.f) - 0.6931471805599453f * __builtin_amdgcn_logf(1.0f + __builtin_amdgcn_exp2f(-1.4426950408889634f * fabsf(x)));
;             run += ls * (1.0f / 16.0f); c[i2 + ii] = run; } }
	s_nop 0
	v_mul_f32_e32 v87, v62, v87
	v_fmac_f32_e32 v87, v59, v86
	v_fmac_f32_e32 v87, v66, v88
	v_fmac_f32_e32 v87, v63, v89
	v_add_f32_e32 v86, v75, v87
	v_mul_f32_e32 v87, v64, v127
	v_fmac_f32_e32 v87, v60, v126
	v_fmac_f32_e32 v87, v69, v128
	v_fmac_f32_e32 v87, v67, v129
	v_add_f32_e32 v86, v87, v86
	v_mul_f32_e32 v87, v68, v139
	v_fmac_f32_e32 v87, v61, v138
	v_fmac_f32_e32 v87, v74, v140
	v_fmac_f32_e32 v87, v71, v141
	v_add_f32_e32 v86, v87, v86
	v_mul_f32_e32 v87, v72, v143
	v_fmac_f32_e32 v87, v65, v142
	v_fmac_f32_e32 v87, v73, v144
	v_fmac_f32_e32 v87, v70, v145
	v_add_f32_e32 v86, v87, v86
	v_min_f32_e32 v87, 0, v86
	v_mul_f32_e64 v86, |v86|, s14
	v_exp_f32_e32 v86, v86
	v_mul_f32_e32 v88, v64, v119
	v_fmac_f32_e32 v88, v60, v118
	v_fmac_f32_e32 v88, v69, v120
	v_add_f32_e32 v86, 1.0, v86
	v_log_f32_e32 v86, v86
	v_fmac_f32_e32 v88, v67, v121
	v_mul_f32_e32 v89, v64, v103
	v_fmac_f32_e32 v89, v60, v102
	v_fmac_f32_e32 v87, 0xbf317218, v86
	v_fmamk_f32 v86, v87, 0x3d800000, v85
	v_mul_f32_e32 v87, v62, v123
	v_fmac_f32_e32 v87, v59, v122
	v_fmac_f32_e32 v87, v66, v124
	v_fmac_f32_e32 v87, v63, v125
	v_add_f32_e32 v87, v75, v87
	v_add_f32_e32 v87, v88, v87
	v_mul_f32_e32 v88, v68, v115
	v_fmac_f32_e32 v88, v61, v114
	v_fmac_f32_e32 v88, v74, v116
	v_fmac_f32_e32 v88, v71, v117
	v_add_f32_e32 v87, v88, v87
	v_mul_f32_e32 v88, v72, v111
	v_fmac_f32_e32 v88, v65, v110
	v_fmac_f32_e32 v88, v73, v112
	v_fmac_f32_e32 v88, v70, v113
	v_add_f32_e32 v87, v88, v87
	v_min_f32_e32 v88, 0, v87
	v_mul_f32_e64 v87, |v87|, s14
	v_exp_f32_e32 v87, v87
	v_fmac_f32_e32 v89, v69, v104
	v_fmac_f32_e32 v89, v67, v105
	v_mul_f32_e32 v43, v64, v43
	v_add_f32_e32 v87, 1.0, v87
	v_log_f32_e32 v87, v87
	v_fmac_f32_e32 v43, v60, v42
	v_mul_f32_e32 v39, v68, v39
	v_fmac_f32_e32 v43, v69, v44
	v_fmac_f32_e32 v88, 0xbf317218, v87
	v_fmamk_f32 v87, v88, 0x3d800000, v86
	v_mul_f32_e32 v88, v62, v107
	v_fmac_f32_e32 v88, v59, v106
	v_fmac_f32_e32 v88, v66, v108
	v_fmac_f32_e32 v88, v63, v109
	v_add_f32_e32 v88, v75, v88
	v_add_f32_e32 v88, v89, v88
	v_mul_f32_e32 v89, v68, v99
	v_fmac_f32_e32 v89, v61, v98
	v_fmac_f32_e32 v89, v74, v100
	v_fmac_f32_e32 v89, v71, v101
	v_add_f32_e32 v88, v89, v88
	v_mul_f32_e32 v89, v72, v95
	v_fmac_f32_e32 v89, v65, v94
	v_fmac_f32_e32 v89, v73, v96
	v_fmac_f32_e32 v89, v70, v97
	v_add_f32_e32 v88, v89, v88
	v_min_f32_e32 v89, 0, v88
	v_mul_f32_e64 v88, |v88|, s14
	v_exp_f32_e32 v88, v88
	v_fmac_f32_e32 v39, v61, v38
	v_mul_f32_e32 v35, v72, v35
	v_fmac_f32_e32 v43, v67, v45
	v_add_f32_e32 v88, 1.0, v88
	v_log_f32_e32 v88, v88
	v_fmac_f32_e32 v39, v74, v40
	v_fmac_f32_e32 v35, v65, v34
	v_fmac_f32_e32 v39, v71, v41
	v_fmac_f32_e32 v89, 0xbf317218, v88
	v_fmamk_f32 v88, v89, 0x3d800000, v87
	v_mul_f32_e32 v89, v62, v91
	v_fmac_f32_e32 v89, v59, v90
	v_fmac_f32_e32 v89, v66, v92
	v_fmac_f32_e32 v89, v63, v93
	v_add_f32_e32 v89, v75, v89
	v_add_f32_e32 v42, v43, v89
	v_fmac_f32_e32 v35, v73, v36
	v_add_f32_e32 v38, v39, v42
	v_fmac_f32_e32 v35, v70, v37
	v_add_f32_e32 v34, v35, v38
	v_min_f32_e32 v35, 0, v34
	v_mul_f32_e64 v34, |v34|, s14
	v_exp_f32_e32 v34, v34
	s_nop 0
	v_add_f32_e32 v34, 1.0, v34
	v_log_f32_e32 v34, v34
	s_nop 0
	v_fmac_f32_e32 v35, 0xbf317218, v34
	v_fmamk_f32 v42, v35, 0x3d800000, v88
	ds_read_b128 v[34:37], v81 offset:1008
	ds_read_b128 v[38:41], v81 offset:992
	ds_read_b128 v[90:93], v81 offset:976
	ds_read_b128 v[94:97], v81 offset:960
	ds_read_b128 v[98:101], v81 offset:944
	ds_read_b128 v[102:105], v81 offset:928
	ds_read_b128 v[106:109], v81 offset:912
	ds_read_b128 v[110:113], v81 offset:896
	ds_read_b128 v[114:117], v81 offset:880
	ds_read_b128 v[118:121], v81 offset:864
	ds_read_b128 v[122:125], v81 offset:848
	ds_read_b128 v[126:129], v81 offset:832
	ds_read_b128 v[138:141], v81 offset:768
	ds_read_b128 v[142:145], v81 offset:784
	ds_read_b128 v[146:149], v81 offset:800
	ds_read_b128 v[150:153], v81 offset:816
	s_waitcnt lgkmcnt(0)
; #define LAS __attribute__((address_space(3)))
; __device__ __forceinline__ void gla_cum(LAS unsigned char* lds, const GlaPre pre, const float (&wa)[16], const float ba, int tid) {
;     ...
;     for (int i2 = 0; i2 < 16; i2 += 4) {
;         f32x4 bb[16];
; #pragma unroll
;         for (int e = 0; e < 16; ++e) bb[e] = *(const LAS f32x4*)(blr + (16 * q + i2 + (e >> 2)) * 16 + 4 * (e & 3));
;         asm volatile("" : "+v"(bb[0]), "+v"(bb[1]), "+v"(bb[2]), "+v"(bb[3]), "+v"(bb[4]), "+v"(bb[5]), "+v"(bb[6]), "+v"(bb[7]), "+v"(bb[8]), "+v"(bb[9]), "+v"(bb[10]), "+v"(bb[11]), "+v"(bb[12]), "+v"(bb[13]), "+v"(bb[14]), "+v"(bb[15]) :: "memory");
; #pragma unroll
;         for (int ii = 0; ii < 4; ++ii) { float x = ba;
; #pragma unroll
;             for (int j4 = 0; j4 < 4; ++j4) { const f32x4 b4 = bb[ii * 4 + j4]; x += b4.x * wa[4 * j4] + b4.y * wa[4 * j4 + 1] + b4.z * wa[4 * j4 + 2] + b4.w * wa[4 * j4 + 3]; }
;             const float ls = fminf(x, 0.f) - 0.6931471805599453f * __builtin_amdgcn_logf(1.0f + __builtin_amdgcn_exp2f(-1.4426950408889634f * fabsf(x)));
;             run += ls * (1.0f / 16.0f); c[i2 + ii] = run; } }
;     tot[q * 128 + k] = run;
;     __syncthreads();
;     float off = 0.f;
; #pragma unroll
;     for (int qq = 0; qq < 3; ++qq) off += (qq < q) ? tot[qq * 128 + k] : 0.f;
	s_nop 0
	v_mul_f32_e32 v43, v62, v139
	v_fmac_f32_e32 v43, v59, v138
	v_mul_f32_e32 v44, v64, v143
	v_fmac_f32_e32 v43, v66, v140
	v_fmac_f32_e32 v44, v60, v142
	v_fmac_f32_e32 v43, v63, v141
	v_fmac_f32_e32 v44, v69, v144
	v_add_f32_e32 v43, v75, v43
	v_fmac_f32_e32 v44, v67, v145
	v_add_f32_e32 v43, v44, v43
	v_mul_f32_e32 v44, v68, v147
	v_fmac_f32_e32 v44, v61, v146
	v_fmac_f32_e32 v44, v74, v148
	v_fmac_f32_e32 v44, v71, v149
	v_add_f32_e32 v43, v44, v43
	v_mul_f32_e32 v44, v72, v151
	v_fmac_f32_e32 v44, v65, v150
	v_fmac_f32_e32 v44, v73, v152
	v_fmac_f32_e32 v44, v70, v153
	v_add_f32_e32 v43, v44, v43
	v_min_f32_e32 v44, 0, v43
	v_mul_f32_e64 v43, |v43|, s14
	v_exp_f32_e32 v43, v43
	v_mul_f32_e32 v45, v64, v123
	v_fmac_f32_e32 v45, v60, v122
	v_fmac_f32_e32 v45, v69, v124
	v_add_f32_e32 v43, 1.0, v43
	v_log_f32_e32 v43, v43
	v_fmac_f32_e32 v45, v67, v125
	v_mul_f32_e32 v81, v64, v107
	v_fmac_f32_e32 v81, v60, v106
	v_fmac_f32_e32 v44, 0xbf317218, v43
	v_fmamk_f32 v43, v44, 0x3d800000, v42
	v_mul_f32_e32 v44, v62, v127
	v_fmac_f32_e32 v44, v59, v126
	v_fmac_f32_e32 v44, v66, v128
	v_fmac_f32_e32 v44, v63, v129
	v_add_f32_e32 v44, v75, v44
	v_add_f32_e32 v44, v45, v44
	v_mul_f32_e32 v45, v68, v119
	v_fmac_f32_e32 v45, v61, v118
	v_fmac_f32_e32 v45, v74, v120
	v_fmac_f32_e32 v45, v71, v121
	v_add_f32_e32 v44, v45, v44
	v_mul_f32_e32 v45, v72, v115
	v_fmac_f32_e32 v45, v65, v114
	v_fmac_f32_e32 v45, v73, v116
	v_fmac_f32_e32 v45, v70, v117
	v_add_f32_e32 v44, v45, v44
	v_min_f32_e32 v45, 0, v44
	v_mul_f32_e64 v44, |v44|, s14
	v_exp_f32_e32 v44, v44
	v_fmac_f32_e32 v81, v69, v108
	v_fmac_f32_e32 v81, v67, v109
	v_mul_f32_e32 v39, v68, v39
	v_add_f32_e32 v44, 1.0, v44
	v_log_f32_e32 v44, v44
	v_fmac_f32_e32 v39, v61, v38
	v_mul_f32_e32 v35, v72, v35
	v_fmac_f32_e32 v39, v74, v40
	v_fmac_f32_e32 v45, 0xbf317218, v44
	v_fmamk_f32 v44, v45, 0x3d800000, v43
	v_mul_f32_e32 v45, v62, v111
	v_fmac_f32_e32 v45, v59, v110
	v_fmac_f32_e32 v45, v66, v112
	v_fmac_f32_e32 v45, v63, v113
	v_add_f32_e32 v45, v75, v45
	v_mul_f32_e32 v62, v62, v95
	v_add_f32_e32 v45, v81, v45
	v_mul_f32_e32 v81, v68, v103
	v_fmac_f32_e32 v62, v59, v94
	v_fmac_f32_e32 v81, v61, v102
	v_fmac_f32_e32 v62, v66, v96
	v_fmac_f32_e32 v81, v74, v104
	v_fmac_f32_e32 v62, v63, v97
	v_fmac_f32_e32 v81, v71, v105
	v_add_f32_e32 v59, v75, v62
	v_mul_f32_e32 v62, v64, v91
	v_add_f32_e32 v45, v81, v45
	v_mul_f32_e32 v81, v72, v99
	v_fmac_f32_e32 v62, v60, v90
	v_fmac_f32_e32 v81, v65, v98
	v_fmac_f32_e32 v62, v69, v92
	v_fmac_f32_e32 v81, v73, v100
	v_fmac_f32_e32 v62, v67, v93
	v_fmac_f32_e32 v35, v65, v34
	v_fmac_f32_e32 v81, v70, v101
	v_add_f32_e32 v59, v62, v59
	v_fmac_f32_e32 v39, v71, v41
	v_fmac_f32_e32 v35, v73, v36
	v_add_f32_e32 v45, v81, v45
	v_add_f32_e32 v38, v39, v59
	v_fmac_f32_e32 v35, v70, v37
	v_min_f32_e32 v81, 0, v45
	v_mul_f32_e64 v45, |v45|, s14
	v_add_f32_e32 v34, v35, v38
	v_exp_f32_e32 v45, v45
	v_min_f32_e32 v35, 0, v34
	v_mul_f32_e64 v34, |v34|, s14
	v_exp_f32_e32 v34, v34
	v_add_f32_e32 v45, 1.0, v45
	v_log_f32_e32 v45, v45
	v_readlane_b32 s14, v254, 45
	v_add_f32_e32 v34, 1.0, v34
	v_log_f32_e32 v34, v34
	v_fmac_f32_e32 v81, 0xbf317218, v45
	v_fmamk_f32 v45, v81, 0x3d800000, v44
	v_add_u32_e32 v36, s14, v57
	v_fmac_f32_e32 v35, 0xbf317218, v34
	v_fmamk_f32 v34, v35, 0x3d800000, v45
	v_and_b32_e32 v35, 0x7f, v133
	ds_write_b32 v36, v34
	v_lshl_add_u32 v37, v35, 2, s14
	v_mov_b32_e32 v36, 0
	s_waitcnt lgkmcnt(0)
	s_barrier
	s_and_saveexec_b64 s[14:15], vcc
	s_cbranch_execz .LBB0_1115
	ds_read_b32 v36, v37
	s_waitcnt lgkmcnt(0)
	v_add_f32_e32 v36, 0, v36
